# combo7 + static priority raise (s_setprio 1) for waves 4-7 during the mLSTM / attention phase
# baseline (speedup 1.0000x reference)
.LBB0_507:
	s_cmp_lt_i32 s48, 4
	s_cselect_b64 s[6:7], -1, 0
	s_and_b64 s[28:29], s[6:7], s[4:5]
	s_andn2_b64 vcc, exec, s[28:29]
	s_cbranch_vccnz .LBB0_561
	v_readfirstlane_b32 s6, v0
	s_nop 3
	s_bitcmp0_b32 s6, 8
	s_cbranch_scc1 .Lprio3_done
	s_setprio 1
.Lprio3_done:
	s_load_dword s4, s[0:1], 0xbc
	s_waitcnt lgkmcnt(0)
	s_bitcmp0_b32 s4, 1
	s_cbranch_scc1 .LBB0_544
	s_cmpk_gt_i32 s2, 0xff
	v_readfirstlane_b32 s8, v0
	s_cbranch_scc1 .LBB0_544
	s_load_dwordx2 s[30:31], s[0:1], 0xb0
	s_waitcnt vmcnt(5)
	v_and_b32_e32 v10, 15, v0
	v_lshlrev_b32_e32 v135, 4, v0
	v_and_b32_e32 v3, 0x1f0, v135
	s_movk_i32 s54, 0x210
	s_waitcnt lgkmcnt(0)
	s_add_u32 s34, s30, 0x33c4a000
	s_addc_u32 s35, s31, 0
	s_add_u32 s36, s30, 0x35c4a000
	s_addc_u32 s37, s31, 0
	s_add_u32 s38, s30, 0x90000
	s_addc_u32 s39, s31, 0
	s_add_u32 s42, s30, 0xd0000
	s_addc_u32 s43, s31, 0
	s_add_u32 s44, s30, 0x110000
	s_addc_u32 s45, s31, 0
	s_add_u32 s6, s30, 0x39c4a000
	s_addc_u32 s7, s31, 0
	s_cmp_lt_u32 s8, 64
	s_cselect_b64 s[46:47], -1, 0
	s_lshr_b32 s9, s8, 3
	s_bfe_u32 s10, s8, 0x10006
	s_and_b32 s52, s9, 0x1ffffff0
	s_and_b32 s56, s8, 0xffffffc0
	s_lshr_b32 s12, s8, 2
	s_add_i32 s53, 0, 0x1f200
	v_or_b32_e32 v6, s52, v10
	s_lshl_b32 s55, s10, 5
	s_add_i32 s58, s56, 0
	s_add_i32 s13, 0, 0x20200
	s_movk_i32 s14, 0x90
	s_add_i32 s18, 0, 0x10800
	v_bfe_u32 v2, v0, 4, 2
	v_mov_b32_e32 v125, 0
	v_add_u32_e32 v12, 0, v3
	v_mul_lo_u32 v3, v6, s54
	v_lshl_or_b32 v149, s10, 4, v10
	v_mul_lo_u32 v6, v6, s14
	s_add_u32 s10, s30, s55
	v_lshlrev_b32_e32 v145, 2, v2
	s_waitcnt vmcnt(3)
	v_add_u32_e32 v18, s18, v6
	s_addc_u32 s11, s31, 0
	v_lshlrev_b32_e32 v6, 1, v10
	v_mov_b32_e32 v7, v125
	v_or_b32_e32 v136, s52, v145
	v_lshl_add_u64 v[8:9], s[10:11], 0, v[6:7]
	v_or_b32_e32 v7, 0x200, v0
	s_lshl_b32 s52, s52, 2
	v_or_b32_e32 v143, s55, v10
	v_lshrrev_b32_e32 v142, 5, v7
	v_or_b32_e32 v7, 0x600, v0
	s_add_i32 s59, 0, 0x1fa00
	s_add_i32 s61, s52, 0
	v_and_b32_e32 v126, 48, v0
	v_mov_b32_e32 v127, v125
	v_lshrrev_b32_e32 v146, 5, v7
	v_or_b32_e32 v7, 16, v143
	s_waitcnt vmcnt(1)
	v_or_b32_e32 v26, 3, v136
	s_add_i32 s60, s59, s52
	s_add_i32 s62, s61, 0x1fc00
	v_lshlrev_b32_e32 v11, 3, v2
	v_lshl_add_u64 v[128:129], s[6:7], 0, v[126:127]
	v_lshrrev_b32_e32 v127, 4, v0
	v_mov_b32_e32 v2, s13
	v_or_b32_e32 v24, 1, v136
	v_or_b32_e32 v25, 2, v136
	v_cmp_gt_u32_e64 s[16:17], v143, v26
	v_cmp_gt_u32_e64 s[24:25], v7, v26
	v_add_u32_e32 v182, s60, v126
	s_add_i32 s60, 0, 0x1fe00
	v_lshlrev_b32_e32 v26, 4, v10
	v_add_u32_e32 v185, s62, v126
	s_add_i32 s62, s61, 0x1fd00
	v_mad_u32_u24 v17, v127, s14, v2
	v_mov_b32_e32 v137, v125
	v_lshl_add_u32 v22, v143, 1, s18
	v_mul_lo_u32 v23, v136, s14
	v_cmp_gt_u32_e64 s[14:15], v143, v25
	v_lshl_add_u32 v27, v7, 1, s18
	v_cmp_gt_u32_e64 s[18:19], v7, v136
	v_cmp_gt_u32_e64 s[20:21], v7, v24
	v_cmp_gt_u32_e64 s[22:23], v7, v25
	v_or_b32_e32 v25, 16, v10
	v_add_u32_e32 v184, s60, v26
	s_add_i32 s60, 0, 0x18f00
	v_add_u32_e32 v186, s62, v126
	s_add_i32 s62, 0, 0x12c00
	v_lshlrev_b32_e32 v7, 2, v7
	v_and_b32_e32 v122, 63, v0
	s_mov_b64 s[26:27], 0x3ec4a000
	v_mul_u32_u24_e32 v181, 0x210, v25
	v_lshlrev_b32_e32 v25, 2, v143
	v_mov_b32_e32 v28, s60
	s_add_i32 s63, s62, s56
	v_add_u32_e32 v189, s59, v7
	v_add_u32_e32 v192, s53, v7
	v_mov_b32_e32 v7, s62
	v_lshlrev_b64 v[154:155], 11, v[136:137]
	v_lshlrev_b32_e32 v1, 3, v0
	v_lshlrev_b32_e32 v133, 2, v10
	v_lshlrev_b32_e32 v124, 3, v10
	v_lshlrev_b32_e32 v132, 2, v122
	v_add_u32_e32 v13, 0, v3
	v_bfe_u32 v3, v0, 2, 2
	v_mul_u32_u24_e32 v153, 0x210, v10
	v_cmp_eq_u32_e32 vcc, 0, v10
	v_lshl_add_u64 v[138:139], v[8:9], 0, s[26:27]
	v_add_u32_e32 v8, s13, v126
	v_and_or_b32 v180, s12, 16, v10
	v_cmp_gt_u32_e64 s[12:13], v143, v24
	v_mul_u32_u24_e32 v24, 0x90, v10
	v_add_u32_e32 v183, s59, v25
	v_mad_u32_u24 v29, v149, s54, v28
	v_mad_u32_u24 v28, v10, s54, v28
	v_add_u32_e32 v187, s63, v11
	s_add_i32 s63, s58, 0x12c20
	v_add_u32_e32 v191, s53, v25
	v_mad_u32_u24 v25, v149, s54, v7
	v_mad_u32_u24 v10, v10, s54, v7
	v_or3_b32 v6, v154, s55, v6
	v_mov_b32_e32 v7, v155
	v_add_u32_e32 v141, s53, v132
	v_or_b32_e32 v15, v11, v3
	v_and_b32_e32 v3, 24, v1
	v_mov_b32_e32 v2, 0x3f803f80
	v_lshrrev_b32_e32 v140, 5, v0
	v_add_u32_e32 v188, s63, v11
	s_add_i32 s63, s53, s52
	s_add_i32 s53, 0, 0x1f600
	v_lshl_add_u64 v[156:157], v[6:7], 0, s[26:27]
	v_mbcnt_lo_u32_b32 v6, -1, 0
	s_movk_i32 s4, 0x1b0
	v_add_u32_e32 v14, 0, v126
	v_add_u32_e32 v16, s58, v3
	v_cndmask_b32_e32 v2, 0, v2, vcc
	v_mul_u32_u24_e32 v9, 0x210, v140
	v_mul_u32_u24_e32 v19, 0x210, v142
	v_mul_u32_u24_e32 v20, 0x210, v146
	v_mul_u32_u24_e32 v21, 0x210, v143
	v_mul_u32_u24_e32 v15, 0x210, v15
	v_add_u32_e32 v193, s53, v26
	s_add_i32 s53, s61, 0x1f400
	s_add_i32 s61, s61, 0x1f500
	s_add_i32 s60, s60, s56
	s_add_i32 s58, s58, 0x18f20
	v_mbcnt_hi_u32_b32 v208, -1, v6
	v_bfrev_b32_e32 v6, 0.5
	v_cmp_gt_u32_e64 s[4:5], s4, v0
	s_mov_b32 s57, 0
	v_and_b32_e32 v123, 0xf8, v1
	v_lshl_add_u64 v[130:131], s[6:7], 0, v[124:125]
	v_cmp_eq_u32_e64 s[6:7], 0, v122
	v_or_b32_e32 v134, 64, v122
	v_cmp_gt_u32_e64 s[8:9], 16, v0
	v_mul_u32_u24_e32 v151, 0x210, v149
	v_mov_b32_e32 v3, v2
	v_mov_b32_e32 v4, v2
	v_mov_b32_e32 v5, v2
	v_or_b32_e32 v144, 32, v140
	v_mov_b32_e32 v147, v125
	v_cmp_gt_u32_e64 s[10:11], v143, v136
	v_add_u32_e32 v190, s63, v126
	v_add_u32_e32 v194, s53, v126
	v_add_u32_e32 v195, s61, v126
	v_add_u32_e32 v196, s60, v11
	v_add_u32_e32 v197, s58, v11
	v_add_u32_e32 v198, s59, v132
	v_or_b32_e32 v199, 0xfffffe00, v0
	v_add_u32_e32 v200, s62, v135
	v_lshlrev_b32_e32 v148, 11, v140
	s_lshl_b32 s53, s2, 8
	s_lshl_b32 s54, s3, 8
	v_lshlrev_b32_e32 v150, 11, v142
	v_lshlrev_b32_e32 v152, 11, v146
	s_lshl_b32 s55, s2, 2
	s_lshl_b32 s74, s3, 2
	v_or_b32_e32 v158, 0x39c52000, v124
	v_mov_b32_e32 v159, v125
	s_movk_i32 s75, 0x42f
	s_add_i32 s76, 0, 0x1f700
	s_mov_b32 s77, 0x33c8a000
	s_mov_b32 s78, 0x35c8a000
	s_mov_b64 s[58:59], 0x100
	s_mov_b64 s[60:61], 0x20000
	s_mov_b64 s[62:63], 0x8000
	v_add_u32_e32 v201, v25, v126
	v_add_u32_e32 v202, v10, v126
	s_mov_b64 s[64:65], 0x3c0000
	s_add_i32 s79, 0, 0x1ff00
	v_add_u32_e32 v203, v29, v126
	v_add_u32_e32 v204, v28, v126
	s_mov_b32 s80, 0x3e0000
	s_mov_b32 s81, 0x3e1000
	v_mov_b32_e32 v224, v125
	v_mov_b32_e32 v225, v125
	v_mov_b32_e32 v226, v125
	v_mov_b32_e32 v227, v125
	v_add_u32_e32 v205, v12, v9
	v_add_u32_e32 v206, v12, v19
	v_add_u32_e32 v207, v12, v20
	v_lshl_or_b32 v209, v208, 2, v6
	v_add_u32_e32 v210, v13, v126
	v_add_u32_e32 v211, v14, v21
	v_add_u32_e32 v212, v16, v15
	v_add_u32_e32 v213, v22, v23
	v_add_u32_e32 v214, v27, v23
	v_add_u32_e32 v215, v17, v124
	v_add_u32_e32 v216, v18, v126
	v_add_u32_e32 v217, v8, v24
	s_mov_b32 s82, s2
	s_mov_b32 s83, s2
	s_branch .LBB0_512

.LBB0_561:
	s_setprio 0
	s_cmp_gt_i32 s49, 4
	s_cselect_b64 s[4:5], -1, 0
	s_and_b64 s[6:7], s[28:29], s[4:5]
	s_andn2_b64 vcc, exec, s[6:7]
	s_cbranch_vccnz .LBB0_615
	s_waitcnt vmcnt(0)
	s_barrier
	s_and_saveexec_b64 s[6:7], s[40:41]
	s_cbranch_execz .LBB0_614
	s_add_i32 s8, 0, 0x24000
	v_mov_b32_e32 v1, s8
	s_waitcnt vmcnt(0) expcnt(0) lgkmcnt(0)
	ds_read_b32 v3, v1
	s_add_i32 s8, 0, 0x24004
	v_mov_b32_e32 v1, s8
	ds_read_b32 v1, v1
	s_waitcnt lgkmcnt(1)
	v_cmp_ne_u32_e32 vcc, 0, v3
	s_cbranch_vccnz .LBB0_578
	s_load_dwordx2 s[12:13], s[92:93], 0x4
	s_add_u32 s8, s50, 0x1000
	s_addc_u32 s9, s51, 0
	s_add_u32 s10, s50, 0x1100
	s_addc_u32 s11, s51, 0
	s_waitcnt lgkmcnt(0)
	s_mul_i32 s22, s12, s3
	s_add_u32 s12, s50, 0x1200
	s_mul_i32 s22, s22, s13
	s_addc_u32 s13, s51, 0
	s_add_u32 s14, s50, 0x1300
	s_addc_u32 s15, s51, 0
	s_mov_b32 s23, 1
	v_mov_b32_e32 v17, 0
	s_branch .LBB0_566
